# speedup vs baseline: 1.0085x; 1.0047x over previous
_Z11prep_kernel8PrepArgs:
	v_lshrrev_b32_e32 v66, 6, v0
	v_mov_b32_e32 v1, 0
	v_mov_b32_e32 v172, 0
	v_and_b32_e32 v67, 63, v0
	v_cmp_eq_u32_e64 s[8:9], 3, v66
	s_and_saveexec_b64 s[4:5], s[8:9]
	s_cbranch_execz .LBB1_2
	s_getpc_b64 s[6:7]
	s_and_b32 s6, s6, 0xffffff80
	v_lshlrev_b32_e32 v2, 7, v67
	v_mov_b32_e32 v3, 0
	v_lshl_add_u64 v[2:3], s[6:7], 0, v[2:3]
	v_add_co_u32_e32 v4, vcc, 0x2000, v2
	s_nop 1
	v_addc_co_u32_e32 v5, vcc, 0, v3, vcc
	v_add_co_u32_e32 v6, vcc, 0x4000, v2
	s_nop 1
	v_addc_co_u32_e32 v7, vcc, 0, v3, vcc
	v_add_co_u32_e32 v8, vcc, 0x6000, v2
	s_nop 1
	v_addc_co_u32_e32 v9, vcc, 0, v3, vcc
	global_load_dword v250, v[2:3], off
	global_load_dword v251, v[4:5], off
	global_load_dword v252, v[6:7], off
	global_load_dword v253, v[8:9], off
.LBB1_2:
	s_or_b64 exec, exec, s[4:5]
	s_load_dwordx16 s[12:27], s[0:1], 0x10
	s_load_dwordx2 s[58:59], s[0:1], 0x0
	s_movk_i32 s3, 0xc0
	v_lshlrev_b32_e32 v173, 2, v172
	v_cmp_gt_u32_e64 s[4:5], s3, v0
	s_movk_i32 s3, 0xbf
	v_add_u32_e32 v166, 0x9000, v173
	v_add_u32_e32 v165, 0xf400, v173
	s_bfe_u32 s30, s2, 0x30003
	v_cmp_lt_u32_e64 s[6:7], s3, v0
	s_and_saveexec_b64 s[10:11], s[6:7]
	s_xor_b64 s[10:11], exec, s[10:11]
	s_cbranch_execz .LBB1_8
	s_movk_i32 s3, 0x11f
	v_cmp_lt_u32_e32 vcc, s3, v0
	s_mul_i32 s3, s30, 0x60
	s_and_saveexec_b64 s[28:29], vcc
	s_xor_b64 s[28:29], exec, s[28:29]
	s_cbranch_execz .LBB1_5
	v_add_u32_e32 v6, 0xfffffee0, v0
	v_add_u32_e32 v4, s3, v6
	s_waitcnt lgkmcnt(0)
	v_mov_b32_e32 v2, s16
	v_mov_b32_e32 v3, s17
	v_add_u32_e32 v7, 0x300, v4
	v_lshlrev_b32_e32 v4, 2, v4
	v_mov_b32_e32 v5, 0
	v_lshl_add_u64 v[2:3], v[4:5], 2, v[2:3]
	v_add_u32_e32 v10, 0xc00, v4
	v_lshl_add_u32 v116, v6, 2, v166

.LBB1_8:
	s_or_saveexec_b64 s[10:11], s[10:11]
	s_waitcnt lgkmcnt(0)
	s_mov_b64 s[16:17], s[58:59]
	s_lshl_b32 s60, s30, 2
	s_load_dword s61, s[20:21], s60
	s_load_dword s62, s[22:23], s60
	s_xor_b64 exec, exec, s[10:11]
	s_mul_i32 s3, s30, 0xc0
	v_add_u32_e32 v4, s3, v0
	v_lshlrev_b32_e32 v2, 4, v4
	v_mov_b32_e32 v3, 0
	v_mov_b32_e32 v5, 0x1800
	v_add_u32_e32 v7, 0x600, v4
	v_lshl_add_u64 v[2:3], s[18:19], 0, v[2:3]
	v_lshl_add_u32 v10, v4, 2, v5
	v_mov_b32_e32 v116, -1
	s_or_b64 exec, exec, s[10:11]
	global_load_dwordx4 v[2:5], v[2:3], off
	s_ashr_i32 s10, s2, 6
	s_and_b32 s3, s2, 7
	s_ashr_i32 s11, s10, 31
	s_lshl_b64 s[18:19], s[10:11], 9
	s_lshl_b32 s11, s3, 6
	s_or_b32 s11, s18, s11
	v_mov_b32_e32 v6, 0
	v_mov_b32_e32 v50, 0
	s_and_saveexec_b64 s[14:15], s[8:9]
	s_cbranch_execz .LBB1_12
	v_or_b32_e32 v6, s11, v67
	s_movk_i32 s18, 0x2580
	s_waitcnt lgkmcnt(0)
	v_mov_b64_e32 v[8:9], s[16:17]
	s_mul_i32 s28, s19, 0x2580
	v_mad_u64_u32 v[8:9], s[18:19], v6, s18, v[8:9]
	v_add_u32_e32 v9, s28, v9
	s_lshl_b32 s18, s30, 1
	s_mov_b32 s19, 0
	v_lshl_add_u64 v[8:9], v[8:9], 0, s[18:19]
	v_add_co_u32_e32 v8, vcc, 0x2000, v8
	s_nop 1
	v_addc_co_u32_e32 v9, vcc, 0, v9, vcc
	global_load_ushort v245, v[8:9], off offset:1024
	global_load_ushort v246, v[8:9], off offset:1040


.LBB1_12:
	s_or_b64 exec, exec, s[14:15]
	s_waitcnt lgkmcnt(0)
	s_and_b32 s17, s17, 0xffff
	s_mov_b32 s19, 0x20000
	s_mov_b32 s18, 0x12c0000
	v_lshlrev_b32_e32 v51, 1, v7
	s_cmp_lg_u32 s3, 0
	s_mulk_i32 s11, 0x2580
	s_cbranch_scc0 .LBB1_167
	s_add_i32 s15, s11, 0xffffb500
	s_add_i32 s14, s11, 0xffff8f80
	s_add_i32 s28, s11, 0xffffda80
	buffer_load_ushort v242, v51, s[16:19], s15 offen
	buffer_load_ushort v243, v51, s[16:19], s28 offen
	buffer_load_ushort v244, v51, s[16:19], s14 offen


	s_mul_hi_i32 s14, s10, 0x9c000
	s_mul_i32 s15, s10, 0x9c000
	s_cbranch_execnz .LBB1_15

.LBB1_15:
	s_add_i32 s10, s11, 0x2580
	s_add_i32 s12, s11, 0x4b00
	s_add_i32 s13, s11, 0x7080
	s_add_i32 s28, s11, 0x9600
	s_add_i32 s29, s11, 0xbb80
	s_add_i32 s31, s11, 0xe100
	s_add_i32 s33, s11, 0x10680
	buffer_load_ushort v20, v51, s[16:19], s11 offen
	buffer_load_ushort v22, v51, s[16:19], s10 offen
	buffer_load_ushort v18, v51, s[16:19], s12 offen
	buffer_load_ushort v21, v51, s[16:19], s13 offen
	buffer_load_ushort v16, v51, s[16:19], s28 offen
	buffer_load_ushort v19, v51, s[16:19], s29 offen
	buffer_load_ushort v15, v51, s[16:19], s31 offen
	buffer_load_ushort v17, v51, s[16:19], s33 offen
	s_add_i32 s10, s11, 0x12c00
	s_add_i32 s12, s11, 0x15180
	s_add_i32 s13, s11, 0x17700
	s_add_i32 s28, s11, 0x19c80
	s_add_i32 s29, s11, 0x1c200
	s_add_i32 s31, s11, 0x1e780
	s_add_i32 s33, s11, 0x20d00
	s_add_i32 s34, s11, 0x23280
	buffer_load_ushort v28, v51, s[16:19], s10 offen
	buffer_load_ushort v30, v51, s[16:19], s12 offen
	buffer_load_ushort v26, v51, s[16:19], s13 offen
	buffer_load_ushort v29, v51, s[16:19], s28 offen
	buffer_load_ushort v24, v51, s[16:19], s29 offen
	buffer_load_ushort v27, v51, s[16:19], s31 offen
	buffer_load_ushort v23, v51, s[16:19], s33 offen
	buffer_load_ushort v25, v51, s[16:19], s34 offen
	s_add_i32 s10, s11, 0x25800
	s_add_i32 s12, s11, 0x27d80
	s_add_i32 s13, s11, 0x2a300
	s_add_i32 s28, s11, 0x2c880
	s_add_i32 s29, s11, 0x2ee00
	s_add_i32 s31, s11, 0x31380
	s_add_i32 s33, s11, 0x33900
	s_add_i32 s34, s11, 0x35e80
	buffer_load_ushort v36, v51, s[16:19], s10 offen
	buffer_load_ushort v38, v51, s[16:19], s12 offen
	buffer_load_ushort v34, v51, s[16:19], s13 offen
	buffer_load_ushort v37, v51, s[16:19], s28 offen
	buffer_load_ushort v32, v51, s[16:19], s29 offen
	buffer_load_ushort v35, v51, s[16:19], s31 offen
	buffer_load_ushort v31, v51, s[16:19], s33 offen
	buffer_load_ushort v33, v51, s[16:19], s34 offen
	s_add_i32 s10, s11, 0x38400
	s_add_i32 s12, s11, 0x3a980
	s_add_i32 s13, s11, 0x3cf00
	s_add_i32 s28, s11, 0x3f480
	s_add_i32 s29, s11, 0x41a00
	s_add_i32 s31, s11, 0x43f80
	s_add_i32 s33, s11, 0x46500
	s_add_i32 s34, s11, 0x48a80
	buffer_load_ushort v44, v51, s[16:19], s10 offen
	buffer_load_ushort v46, v51, s[16:19], s12 offen
	buffer_load_ushort v42, v51, s[16:19], s13 offen
	buffer_load_ushort v45, v51, s[16:19], s28 offen
	buffer_load_ushort v40, v51, s[16:19], s29 offen
	buffer_load_ushort v43, v51, s[16:19], s31 offen
	buffer_load_ushort v39, v51, s[16:19], s33 offen
	buffer_load_ushort v41, v51, s[16:19], s34 offen
	s_add_i32 s10, s11, 0x4b000
	s_add_i32 s12, s11, 0x4d580
	s_add_i32 s13, s11, 0x4fb00
	s_add_i32 s28, s11, 0x52080
	s_add_i32 s29, s11, 0x54600
	s_add_i32 s31, s11, 0x56b80
	s_add_i32 s33, s11, 0x59100
	s_add_i32 s34, s11, 0x5b680
	buffer_load_ushort v48, v51, s[16:19], s10 offen
	buffer_load_ushort v49, v51, s[16:19], s12 offen
	buffer_load_ushort v70, v51, s[16:19], s13 offen
	buffer_load_ushort v72, v51, s[16:19], s28 offen
	buffer_load_ushort v68, v51, s[16:19], s29 offen
	buffer_load_ushort v71, v51, s[16:19], s31 offen
	buffer_load_ushort v47, v51, s[16:19], s33 offen
	buffer_load_ushort v69, v51, s[16:19], s34 offen
	s_add_i32 s10, s11, 0x5dc00
	s_add_i32 s12, s11, 0x60180
	s_add_i32 s13, s11, 0x62700
	s_add_i32 s28, s11, 0x64c80
	s_add_i32 s29, s11, 0x67200
	s_add_i32 s31, s11, 0x69780
	s_add_i32 s33, s11, 0x6bd00
	s_add_i32 s34, s11, 0x6e280
	buffer_load_ushort v78, v51, s[16:19], s10 offen
	buffer_load_ushort v80, v51, s[16:19], s12 offen
	buffer_load_ushort v76, v51, s[16:19], s13 offen
	buffer_load_ushort v79, v51, s[16:19], s28 offen
	buffer_load_ushort v74, v51, s[16:19], s29 offen
	buffer_load_ushort v77, v51, s[16:19], s31 offen
	buffer_load_ushort v73, v51, s[16:19], s33 offen
	buffer_load_ushort v75, v51, s[16:19], s34 offen
	s_add_i32 s10, s11, 0x70800
	s_add_i32 s12, s11, 0x72d80
	s_add_i32 s13, s11, 0x75300
	s_add_i32 s28, s11, 0x77880
	s_add_i32 s29, s11, 0x79e00
	s_add_i32 s31, s11, 0x7c380
	s_add_i32 s33, s11, 0x7e900
	s_add_i32 s34, s11, 0x80e80
	buffer_load_ushort v87, v51, s[16:19], s10 offen
	buffer_load_ushort v89, v51, s[16:19], s12 offen
	buffer_load_ushort v85, v51, s[16:19], s13 offen
	buffer_load_ushort v88, v51, s[16:19], s28 offen
	buffer_load_ushort v83, v51, s[16:19], s29 offen
	buffer_load_ushort v86, v51, s[16:19], s31 offen
	buffer_load_ushort v82, v51, s[16:19], s33 offen
	buffer_load_ushort v84, v51, s[16:19], s34 offen
	s_add_i32 s10, s11, 0x83400
	s_add_i32 s12, s11, 0x85980
	s_add_i32 s13, s11, 0x87f00
	s_add_i32 s28, s11, 0x8a480
	s_add_i32 s29, s11, 0x8ca00
	s_add_i32 s31, s11, 0x8ef80
	s_add_i32 s33, s11, 0x91500
	s_add_i32 s11, s11, 0x93a80
	buffer_load_ushort v90, v51, s[16:19], s10 offen
	buffer_load_ushort v92, v51, s[16:19], s12 offen
	buffer_load_ushort v81, v51, s[16:19], s13 offen
	buffer_load_ushort v91, v51, s[16:19], s28 offen
	buffer_load_ushort v9, v51, s[16:19], s29 offen
	buffer_load_ushort v7, v51, s[16:19], s31 offen
	buffer_load_ushort v8, v51, s[16:19], s33 offen
	buffer_load_ushort v11, v51, s[16:19], s11 offen
	s_waitcnt vmcnt(63)
	s_and_b32 s63, s2, 7
	s_cmp_eq_u32 s63, 0
	s_cbranch_scc1 .Lp1_zdone
	v_cvt_f32_f16_e32 v14, v242
	v_cvt_f32_f16_e32 v13, v243
	v_cvt_f32_f16_e32 v12, v244
.Lp1_zdone:
	v_add_u32_e32 v164, 0x24600, v173
	v_add_u32_e32 v119, 0x24800, v173
	v_add_u32_e32 v117, 0x24700, v173
	s_and_saveexec_b64 s[10:11], s[8:9]
	s_cbranch_execz .LBB1_19
	s_lshl_b32 s12, s30, 2
	v_cvt_f32_f16_e32 v50, v245
	v_cvt_f32_f16_e32 v6, v246
	v_mov_b32_e32 v51, s61
	s_mov_b32 s8, 0x41a00000

	v_add_f32_e32 v50, v50, v51
	v_cmp_nlt_f32_e32 vcc, s8, v50
	s_and_saveexec_b64 s[8:9], vcc
	s_cbranch_execz .LBB1_18
	v_mul_f32_e32 v51, 0x3fb8aa3b, v50
	s_mov_b32 s13, 0x3fb8aa3b
	v_rndne_f32_e32 v52, v51
	v_sub_f32_e32 v53, v51, v52
	v_fma_f32 v51, v50, s13, -v51
	v_fmamk_f32 v51, v50, 0x32a5705f, v51
	v_add_f32_e32 v51, v53, v51
	v_exp_f32_e32 v51, v51
	v_cvt_i32_f32_e32 v52, v52
	s_mov_b32 s13, 0xc2ce8ed0
	v_cmp_ngt_f32_e32 vcc, s13, v50
	s_mov_b32 s13, 0x42b17218
	v_ldexp_f32 v51, v51, v52
	v_cndmask_b32_e32 v51, 0, v51, vcc
	v_mov_b32_e32 v64, 0x7f800000
	v_cmp_nlt_f32_e32 vcc, s13, v50
	s_mov_b32 s13, 0x3f2aaaab
	s_mov_b32 s16, 0x7f800000
	v_cndmask_b32_e32 v65, v64, v51, vcc
	v_add_f32_e32 v52, 1.0, v65
	v_add_f32_e32 v50, -1.0, v52
	v_sub_f32_e32 v51, v50, v52
	v_add_f32_e32 v51, 1.0, v51
	v_sub_f32_e32 v50, v65, v50
	v_add_f32_e32 v53, v50, v51
	v_frexp_mant_f32_e32 v54, v52
	v_cvt_f64_f32_e32 v[50:51], v52
	v_frexp_exp_i32_f64_e32 v50, v[50:51]
	v_cmp_gt_f32_e32 vcc, s13, v54
	s_mov_b32 s13, 0x3f317218
	s_nop 0
	v_subbrev_co_u32_e32 v58, vcc, 0, v50, vcc
	v_sub_u32_e32 v50, 0, v58
	v_ldexp_f32 v51, v52, v50
	v_add_f32_e32 v52, -1.0, v51
	v_add_f32_e32 v54, 1.0, v51
	v_ldexp_f32 v50, v53, v50
	v_add_f32_e32 v53, 1.0, v52
	v_add_f32_e32 v55, -1.0, v54
	v_sub_f32_e32 v53, v51, v53
	v_sub_f32_e32 v51, v51, v55
	v_add_f32_e32 v53, v50, v53
	v_add_f32_e32 v50, v50, v51
	v_add_f32_e32 v59, v54, v50
	v_rcp_f32_e32 v61, v59
	v_sub_f32_e32 v51, v54, v59
	v_add_f32_e32 v60, v50, v51
	v_add_f32_e32 v51, v52, v53
	v_mul_f32_e32 v63, v51, v61
	v_sub_f32_e32 v50, v52, v51
	v_mul_f32_e32 v52, v59, v63
	v_fma_f32 v54, v63, v59, -v52
	v_fmac_f32_e32 v54, v63, v60
	v_add_f32_e32 v62, v53, v50
	v_add_f32_e32 v50, v52, v54
	v_sub_f32_e32 v53, v51, v50
	v_pk_add_f32 v[56:57], v[50:51], v[52:53] neg_lo:[0,1] neg_hi:[0,1]
	v_mov_b32_e32 v55, v50
	v_pk_add_f32 v[50:51], v[56:57], v[54:55] neg_lo:[0,1] neg_hi:[0,1]
	v_cmp_neq_f32_e32 vcc, s16, v65
	v_add_f32_e32 v51, v62, v51
	v_add_f32_e32 v50, v50, v51
	v_add_f32_e32 v51, v53, v50
	v_mul_f32_e32 v62, v61, v51
	v_mul_f32_e32 v52, v59, v62
	v_fma_f32 v54, v62, v59, -v52
	v_fmac_f32_e32 v54, v62, v60
	v_sub_f32_e32 v53, v53, v51
	v_add_f32_e32 v59, v50, v53
	v_add_f32_e32 v50, v52, v54
	v_sub_f32_e32 v53, v51, v50
	v_pk_add_f32 v[56:57], v[50:51], v[52:53] neg_lo:[0,1] neg_hi:[0,1]
	v_mov_b32_e32 v55, v50
	v_pk_add_f32 v[50:51], v[56:57], v[54:55] neg_lo:[0,1] neg_hi:[0,1]
	v_cvt_f32_i32_e32 v52, v58
	v_add_f32_e32 v51, v59, v51
	v_add_f32_e32 v50, v50, v51
	v_add_f32_e32 v50, v53, v50
	v_add_f32_e32 v53, v63, v62
	v_sub_f32_e32 v51, v53, v63
	v_mul_f32_e32 v50, v61, v50
	v_sub_f32_e32 v51, v62, v51
	v_add_f32_e32 v50, v51, v50
	v_add_f32_e32 v54, v53, v50
	v_mul_f32_e32 v56, v54, v54
	v_mov_b32_e32 v51, 0x3ecc95a3
	v_sub_f32_e32 v53, v54, v53
	v_fmac_f32_e32 v51, 0x3e9b6dac, v56
	v_sub_f32_e32 v50, v50, v53
	v_fmaak_f32 v51, v56, v51, 0x3f2aaada
	v_ldexp_f32 v57, v50, 1
	v_mul_f32_e32 v53, v54, v56
	v_mov_b32_e32 v50, 0x3f317218
	v_pk_mul_f32 v[50:51], v[52:53], v[50:51]
	v_ldexp_f32 v55, v54, 1
	v_fma_f32 v53, v52, s13, -v50
	v_fmamk_f32 v54, v52, 0xb102e308, v53
	v_pk_add_f32 v[52:53], v[50:51], v[54:55]
	v_mov_b32_e32 v56, v50
	v_sub_f32_e32 v55, v53, v55
	v_sub_f32_e32 v55, v51, v55
	v_add_f32_e32 v57, v57, v55
	v_pk_add_f32 v[50:51], v[52:53], v[50:51] neg_lo:[0,1] neg_hi:[0,1]
	v_pk_add_f32 v[58:59], v[52:53], v[56:57]
	v_mov_b32_e32 v55, v52
	v_mov_b32_e32 v51, v59
	v_pk_add_f32 v[60:61], v[54:55], v[50:51] neg_lo:[0,1] neg_hi:[0,1]
	v_pk_add_f32 v[50:51], v[54:55], v[50:51]
	v_mov_b32_e32 v56, v57
	v_pk_add_f32 v[54:55], v[50:51], v[52:53] op_sel:[1,0] op_sel_hi:[0,1] neg_lo:[0,1] neg_hi:[0,1]
	v_pk_add_f32 v[62:63], v[58:59], v[54:55] op_sel_hi:[1,0] neg_lo:[0,1] neg_hi:[0,1]
	v_mov_b32_e32 v58, v59
	v_mov_b32_e32 v59, v51
	v_pk_mov_b32 v[54:55], v[52:53], v[54:55] op_sel:[1,0]
	v_mov_b32_e32 v57, v52
	v_pk_add_f32 v[54:55], v[58:59], v[54:55] neg_lo:[0,1] neg_hi:[0,1]
	v_mov_b32_e32 v62, v60
	v_pk_add_f32 v[52:53], v[56:57], v[54:55] neg_lo:[0,1] neg_hi:[0,1]
	v_mov_b32_e32 v61, v51
	v_pk_add_f32 v[54:55], v[62:63], v[52:53]
	s_mov_b32 s13, 0x33800000
	v_pk_add_f32 v[56:57], v[54:55], v[54:55] op_sel:[0,1] op_sel_hi:[1,0]
	s_nop 0
	v_pk_add_f32 v[50:51], v[50:51], v[56:57] op_sel:[1,0] op_sel_hi:[0,1]
	v_mov_b32_e32 v55, v50
	v_pk_add_f32 v[58:59], v[54:55], v[60:61] neg_lo:[0,1] neg_hi:[0,1]
	v_mov_b32_e32 v53, v56
	v_sub_f32_e32 v51, v54, v58
	v_pk_add_f32 v[52:53], v[52:53], v[58:59] neg_lo:[0,1] neg_hi:[0,1]
	v_sub_f32_e32 v51, v60, v51
	v_add_f32_e32 v51, v52, v51
	v_add_f32_e32 v51, v51, v53
	v_add_f32_e32 v50, v50, v51
	v_cndmask_b32_e32 v50, v64, v50, vcc
	v_cmp_lt_f32_e64 vcc, |v65|, s13
	s_nop 1
	v_cndmask_b32_e32 v50, v50, v65, vcc
.LBB1_18:
	s_or_b64 exec, exec, s[8:9]

	v_mov_b32_e32 v51, s62
	v_mbcnt_lo_u32_b32 v53, -1, 0
	s_mov_b32 s8, 0x3fb8aa3b
	v_mbcnt_hi_u32_b32 v53, -1, v53
	v_and_b32_e32 v60, 64, v53
	v_add_u32_e32 v61, -1, v53
	v_add_u32_e32 v62, -2, v53
	v_cmp_lt_i32_e32 vcc, v61, v60
	v_add_u32_e32 v63, -4, v53
	v_add_u32_e32 v64, -8, v53
	v_cndmask_b32_e32 v61, v61, v53, vcc
	v_cmp_lt_i32_e32 vcc, v62, v60
	v_add_u32_e32 v65, -16, v53
	v_subrev_u32_e32 v93, 32, v53
	v_cndmask_b32_e32 v62, v62, v53, vcc
	v_cmp_lt_i32_e32 vcc, v63, v60
	s_mov_b32 s9, 0xc2ce8ed0
	s_mov_b32 s12, 0x42b17218
	v_cndmask_b32_e32 v63, v63, v53, vcc
	v_cmp_lt_i32_e32 vcc, v64, v60
	v_mov_b32_e32 v52, 0x7f800000
	s_mov_b32 s13, 0xbfb8aa3b
	v_cndmask_b32_e32 v64, v64, v53, vcc
	v_cmp_lt_i32_e32 vcc, v65, v60
	v_mul_f32_e32 v55, 0xbfb8aa3b, v6
	v_rndne_f32_e32 v57, v55
	v_cndmask_b32_e32 v65, v65, v53, vcc
	v_cmp_lt_i32_e32 vcc, v93, v60
	v_lshlrev_b32_e32 v60, 2, v61
	v_fma_f32 v58, v6, s13, -v55
	v_cndmask_b32_e32 v53, v93, v53, vcc
	v_sub_f32_e32 v55, v55, v57
	v_fmamk_f32 v58, v6, 0xb2a5705f, v58
	v_add_f32_e32 v55, v55, v58
	v_lshlrev_b32_e32 v58, 2, v62
	v_cvt_i32_f32_e32 v57, v57
	v_lshlrev_b32_e32 v62, 2, v63
	v_exp_f32_e32 v55, v55
	s_mov_b32 s16, 0x42ce8ed0
	s_mov_b32 s17, 0xc2b17218
	v_lshlrev_b32_e32 v53, 2, v53
	v_ldexp_f32 v55, v55, v57
	v_lshlrev_b32_e32 v54, 2, v67
	v_add_u32_e32 v59, v119, v54
	v_add_u32_e32 v56, v164, v54

	v_mul_f32_e32 v94, 0x3fb8aa3b, v51
	v_fma_f32 v95, v51, s8, -v94
	v_rndne_f32_e32 v96, v94
	v_fmamk_f32 v95, v51, 0x32a5705f, v95
	v_sub_f32_e32 v94, v94, v96
	v_add_f32_e32 v94, v94, v95
	v_cvt_i32_f32_e32 v96, v96
	v_exp_f32_e32 v94, v94
	v_cmp_ngt_f32_e32 vcc, s9, v51
	v_ldexp_f32 v61, v94, v96
	s_nop 0
	v_cndmask_b32_e32 v61, 0, v61, vcc
	v_cmp_nlt_f32_e32 vcc, s12, v51
	s_nop 1
	v_cndmask_b32_e32 v51, v52, v61, vcc
	v_mul_f32_e64 v61, v50, -v51
	ds_bpermute_b32 v60, v60, v61
	v_cmp_eq_u32_e32 vcc, 0, v67
	s_waitcnt lgkmcnt(0)
	v_fma_f32 v50, v50, -v51, v60
	v_cndmask_b32_e32 v50, v50, v61, vcc
	ds_bpermute_b32 v51, v58, v50
	v_cmp_gt_u32_e32 vcc, 2, v67
	v_lshlrev_b32_e32 v58, 2, v64
	v_lshlrev_b32_e32 v60, 2, v65
	s_waitcnt lgkmcnt(0)
	v_add_f32_e32 v51, v50, v51
	v_cndmask_b32_e32 v50, v51, v50, vcc
	ds_bpermute_b32 v51, v62, v50
	v_cmp_nlt_f32_e32 vcc, s16, v6
	s_waitcnt lgkmcnt(0)
	v_add_f32_e32 v51, v50, v51
	v_cndmask_b32_e32 v55, 0, v55, vcc
	v_cmp_ngt_f32_e32 vcc, s17, v6
	s_nop 1
	v_cndmask_b32_e32 v6, v52, v55, vcc
	v_cmp_gt_u32_e32 vcc, 4, v67
	v_add_f32_e32 v6, 1.0, v6
	v_div_scale_f32 v52, s[8:9], v6, v6, 1.0
	v_cndmask_b32_e32 v50, v51, v50, vcc
	ds_bpermute_b32 v51, v58, v50
	v_cmp_gt_u32_e64 s[8:9], 8, v67
	v_rcp_f32_e32 v57, v52
	v_div_scale_f32 v55, vcc, 1.0, v6, 1.0
	s_waitcnt lgkmcnt(0)
	v_add_f32_e32 v51, v50, v51
	v_cndmask_b32_e64 v50, v51, v50, s[8:9]
	ds_bpermute_b32 v51, v60, v50
	v_cmp_gt_u32_e64 s[8:9], 16, v67
	v_fma_f32 v58, -v52, v57, 1.0
	v_fmac_f32_e32 v57, v58, v57
	v_mul_f32_e32 v58, v55, v57
	s_waitcnt lgkmcnt(0)
	v_add_f32_e32 v51, v50, v51
	v_cndmask_b32_e64 v50, v51, v50, s[8:9]
	ds_bpermute_b32 v51, v53, v50
	v_fma_f32 v60, -v52, v58, v55
	v_fmac_f32_e32 v58, v60, v57
	v_fma_f32 v52, -v52, v58, v55
	v_div_fmas_f32 v52, v52, v57, v58
	s_waitcnt lgkmcnt(0)
	v_add_f32_e32 v51, v50, v51
	v_cmp_gt_u32_e32 vcc, 32, v67
	v_div_fixup_f32 v6, v52, v6, 1.0
	s_nop 0
	v_cndmask_b32_e32 v50, v51, v50, vcc
	v_mul_f32_e32 v51, 0x3fb8aa3b, v50
	v_exp_f32_e32 v51, v51
	ds_write_b32 v59, v6
	ds_write_b32 v56, v50
	v_add_u32_e32 v50, v117, v54
	v_mul_f32_e32 v6, v6, v51
	ds_write_b32 v50, v6
